# P13 route row loop: next-row prefetch waited only at the latch with a counted wait (stores stay in flight); no per-row store drain
# baseline (speedup 1.0000x reference)
.LBB0_1745:
	s_add_i32 s4, s22, s3
	s_min_i32 s29, s4, 0x8000
	s_cmp_ge_i32 s22, s29
	s_cbranch_scc1 .LBB0_1754
	v_mbcnt_lo_u32_b32 v1, -1, 0
	v_mbcnt_hi_u32_b32 v134, -1, v1
	v_and_b32_e32 v1, 64, v134
	v_add_u32_e32 v135, 64, v1
	v_xor_b32_e32 v1, 1, v134
	v_cmp_lt_i32_e32 vcc, v1, v135
	v_xor_b32_e32 v136, 2, v134
	s_add_u32 s6, s50, 0x1000
	v_cndmask_b32_e32 v1, v134, v1, vcc
	v_cmp_lt_i32_e32 vcc, v136, v135
	v_mov_b32_e32 v163, 0
	s_addc_u32 s7, s51, 0
	v_cndmask_b32_e32 v136, v134, v136, vcc
	v_lshlrev_b32_e32 v171, 2, v136
	v_xor_b32_e32 v136, 4, v134
	v_cmp_lt_i32_e32 vcc, v136, v135
	v_lshlrev_b32_e32 v162, 2, v130
	v_lshlrev_b32_e32 v166, 2, v131
	v_cndmask_b32_e32 v136, v134, v136, vcc
	v_lshlrev_b32_e32 v200, 2, v136
	v_xor_b32_e32 v136, 8, v134
	v_cmp_lt_i32_e32 vcc, v136, v135
	v_mov_b32_e32 v167, v163
	v_lshlrev_b32_e32 v172, 2, v132
	v_cndmask_b32_e32 v136, v134, v136, vcc
	v_lshlrev_b32_e32 v202, 2, v136
	v_xor_b32_e32 v136, 16, v134
	v_cmp_lt_i32_e32 vcc, v136, v135
	v_mov_b32_e32 v173, v163
	v_lshlrev_b32_e32 v176, 2, v133
	v_mov_b32_e32 v177, v163
	s_add_u32 s30, s72, 0x140000
	v_cndmask_b32_e32 v136, v134, v136, vcc
	v_lshl_add_u64 v[164:165], s[6:7], 0, v[162:163]
	v_lshl_add_u64 v[168:169], s[6:7], 0, v[166:167]
	v_lshl_add_u64 v[174:175], s[6:7], 0, v[172:173]
	v_lshl_add_u64 v[178:179], s[6:7], 0, v[176:177]
	v_readlane_b32 s6, v254, 6
	s_addc_u32 s31, s73, 0
	v_lshlrev_b32_e32 v203, 2, v136
	v_xor_b32_e32 v136, 32, v134
	v_readlane_b32 s7, v254, 7
	s_lshl_b32 s6, s6, 9
	s_ashr_i32 s23, s22, 31
	v_cmp_lt_i32_e32 vcc, v136, v135
	s_add_i32 s34, s6, 0
	s_lshl_b64 s[6:7], s[22:23], 10
	v_cndmask_b32_e32 v134, v134, v136, vcc
	v_mov_b32_e32 v181, s7
	v_or_b32_e32 v180, s6, v130
	s_lshl_b64 s[6:7], s[22:23], 11
	s_mov_b32 s33, 0
	s_mov_b32 s47, -1
	v_lshlrev_b32_e32 v1, 2, v1
	v_lshlrev_b32_e32 v204, 2, v134
	v_cmp_eq_u32_e64 s[4:5], 0, v250
	s_lshl_b32 s38, s22, 1
	v_lshl_or_b32 v182, v250, 3, s6
	v_mov_b32_e32 v183, s7
	v_mov_b32_e32 v167, 0x358637bd
	s_mov_b32 s23, 0x800000
	s_mov_b32 s35, 0xdd00000
	s_mov_b32 s46, 0xff61b1e6
	v_mov_b32_e32 v173, 1
	s_mov_b64 s[40:41], 0x400
	s_mov_b64 s[42:43], 0x800
	v_mov_b32_e32 v177, 0xff61b1e6
	s_waitcnt vmcnt(0)
	s_branch .LBB0_1748
.LBB0_1747:
	s_or_b64 exec, exec, s[44:45]
	s_waitcnt vmcnt(4)
	s_add_i32 s33, s33, 1
	s_add_i32 s38, s38, 2
	s_add_i32 s6, s22, s33
	v_lshl_add_u64 v[180:181], v[180:181], 0, s[40:41]
	v_lshl_add_u64 v[182:183], v[182:183], 0, s[42:43]
	s_cmp_ge_i32 s6, s29
	v_mov_b32_e32 v193, v184
	v_mov_b32_e32 v201, v185
	v_mov_b32_e32 v198, v186
	v_mov_b32_e32 v199, v187
	v_mov_b32_e32 v196, v188
	v_mov_b32_e32 v197, v189
	v_mov_b32_e32 v194, v190
	v_mov_b32_e32 v195, v191
	s_cbranch_scc1 .LBB0_1754
.LBB0_1748:
	s_add_i32 s6, s22, s33
	s_add_i32 s7, s6, 1
	s_cmp_ge_i32 s7, s29
	v_mov_b32_e32 v184, v193
	v_mov_b32_e32 v185, v201
	v_mov_b32_e32 v186, v198
	v_mov_b32_e32 v187, v199
	v_mov_b32_e32 v188, v196
	v_mov_b32_e32 v189, v197
	v_mov_b32_e32 v190, v194
	v_mov_b32_e32 v191, v195
	s_cbranch_scc1 .LBB0_1750
	v_lshl_add_u64 v[184:185], s[72:73], 0, v[182:183]
	v_add_co_u32_e32 v190, vcc, 0x8c00000, v184
	s_nop 1
	v_addc_co_u32_e32 v191, vcc, 0, v185, vcc
	global_load_dwordx2 v[184:185], v[190:191], off offset:2048
	global_load_dwordx2 v[186:187], v[190:191], off offset:2560
	global_load_dwordx2 v[188:189], v[190:191], off offset:3072
	s_nop 0
	global_load_dwordx2 v[190:191], v[190:191], off offset:3584
.LBB0_1750:
	s_ashr_i32 s7, s6, 31
	s_lshr_b32 s7, s7, 21
	s_add_i32 s6, s6, s7
	s_ashr_i32 s6, s6, 11
	s_cmp_eq_u32 s6, s47
	s_cbranch_scc1 .LBB0_1752
	s_mul_i32 s8, s6, 0x6000
	s_mul_hi_i32 s7, s6, 0x6000
	s_add_u32 s10, s77, s8
	s_addc_u32 s7, s82, s7
	s_add_u32 s8, s10, 0x4000
	s_addc_u32 s9, s7, 0
	global_load_dwordx4 v[146:149], v162, s[8:9]
	global_load_dwordx4 v[150:153], v166, s[8:9]
	global_load_dwordx4 v[154:157], v172, s[8:9]
	global_load_dwordx4 v[158:161], v176, s[8:9]
	s_waitcnt lgkmcnt(2)
	global_load_dwordx4 v[206:209], v[164:165], off
	s_waitcnt lgkmcnt(0)
	global_load_dwordx4 v[210:213], v[168:169], off
	global_load_dwordx4 v[214:217], v[174:175], off
	global_load_dwordx4 v[218:221], v[178:179], off
	s_add_u32 s8, s10, 0x3000
	s_addc_u32 s9, s7, 0
	global_load_dwordx4 v[138:141], v162, s[8:9]
	global_load_dwordx4 v[134:137], v166, s[8:9]
	global_load_dwordx4 v[130:133], v172, s[8:9]
	global_load_dwordx4 v[142:145], v176, s[8:9]
	s_mov_b32 s47, s6
	s_waitcnt vmcnt(11)
	v_pk_add_f32 v[148:149], v[148:149], 1.0 op_sel_hi:[1,0]
	v_pk_add_f32 v[146:147], v[146:147], 1.0 op_sel_hi:[1,0]
	s_waitcnt vmcnt(10)
	v_pk_add_f32 v[152:153], v[152:153], 1.0 op_sel_hi:[1,0]
	v_pk_add_f32 v[150:151], v[150:151], 1.0 op_sel_hi:[1,0]
	s_waitcnt vmcnt(9)
	v_pk_add_f32 v[156:157], v[156:157], 1.0 op_sel_hi:[1,0]
	v_pk_add_f32 v[154:155], v[154:155], 1.0 op_sel_hi:[1,0]
	s_waitcnt vmcnt(8)
	v_pk_add_f32 v[160:161], v[160:161], 1.0 op_sel_hi:[1,0]
	v_pk_add_f32 v[158:159], v[158:159], 1.0 op_sel_hi:[1,0]
	s_waitcnt vmcnt(7)
	v_pk_mul_f32 v[148:149], v[208:209], v[148:149]
	v_pk_mul_f32 v[146:147], v[206:207], v[146:147]
	s_waitcnt vmcnt(6)
	v_pk_mul_f32 v[152:153], v[212:213], v[152:153]
	v_pk_mul_f32 v[150:151], v[210:211], v[150:151]
	s_waitcnt vmcnt(5)
	v_pk_mul_f32 v[156:157], v[216:217], v[156:157]
	v_pk_mul_f32 v[154:155], v[214:215], v[154:155]
	s_waitcnt vmcnt(4)
	v_pk_mul_f32 v[160:161], v[220:221], v[160:161]
	v_pk_mul_f32 v[158:159], v[218:219], v[158:159]
	s_waitcnt vmcnt(0)
.LBB0_1752:
	s_waitcnt lgkmcnt(2)
	v_and_b32_e32 v209, 0xffff0000, v201
	v_and_b32_e32 v208, 0xffff0000, v193
	s_waitcnt lgkmcnt(1)
	v_lshlrev_b32_e32 v211, 16, v199
	v_lshlrev_b32_e32 v210, 16, v198
	v_and_b32_e32 v199, 0xffff0000, v199
	v_and_b32_e32 v198, 0xffff0000, v198
	v_lshlrev_b32_e32 v207, 16, v201
	v_lshlrev_b32_e32 v206, 16, v193
	v_lshlrev_b32_e32 v212, 16, v196
	s_waitcnt lgkmcnt(0)
	v_and_b32_e32 v213, 0xffff0000, v196
	v_lshlrev_b32_e32 v196, 16, v197
	v_lshlrev_b32_e32 v214, 16, v194
	v_pk_mul_f32 v[192:193], v[208:209], v[208:209]
	v_pk_mul_f32 v[216:217], v[198:199], v[198:199]
	v_and_b32_e32 v197, 0xffff0000, v197
	v_pk_fma_f32 v[192:193], v[206:207], v[206:207], v[192:193]
	v_pk_fma_f32 v[216:217], v[210:211], v[210:211], v[216:217]
	v_mul_f32_e32 v215, v212, v212
	v_mul_f32_e32 v219, v213, v213
	v_mul_f32_e32 v170, v196, v196
	v_mov_b32_e32 v218, v214
	v_and_b32_e32 v201, 0xffff0000, v194
	v_lshlrev_b32_e32 v194, 16, v195
	v_and_b32_e32 v195, 0xffff0000, v195
	v_pk_add_f32 v[192:193], v[192:193], v[192:193] op_sel_hi:[0,1]
	v_pk_add_f32 v[216:217], v[216:217], v[216:217] op_sel_hi:[0,1]
	v_pk_fma_f32 v[220:221], v[196:197], v[196:197], v[170:171] op_sel_hi:[1,1,0]
	v_pk_add_f32 v[218:219], v[214:215], v[218:219]
	v_mul_f32_e32 v220, v201, v201
	v_mul_f32_e32 v192, v194, v194
	v_mul_f32_e32 v216, v195, v195
	v_mul_f32_e32 v222, v214, v214
	v_mov_b32_e32 v223, v219
	v_pk_add_f32 v[218:219], v[222:223], v[220:221]
	v_pk_add_f32 v[192:193], v[192:193], v[216:217]
	v_mov_b32_e32 v224, 0
	v_pk_add_f32 v[192:193], v[218:219], v[192:193]
	v_mov_b32_e32 v215, v201
	v_add_f32_e32 v170, v192, v193
	s_nop 1
	v_add_f32_dpp v237, v170, v170 quad_perm:[1,0,3,2] row_mask:0xf bank_mask:0xf
	s_nop 1
	v_add_f32_dpp v237, v237, v237 quad_perm:[2,3,0,1] row_mask:0xf bank_mask:0xf
	s_nop 1
	v_add_f32_dpp v237, v237, v237 row_half_mirror row_mask:0xf bank_mask:0xf
	s_nop 1
	v_add_f32_dpp v237, v237, v237 row_mirror row_mask:0xf bank_mask:0xf
	s_nop 0
	v_mov_b32_e32 v236, v237
	s_nop 1
	v_permlane16_swap_b32_e32 v237, v236
	s_nop 0
	v_add_f32_e32 v237, v237, v236
	v_mov_b32_e32 v236, v237
	s_nop 1
	v_permlane32_swap_b32_e32 v237, v236
	s_nop 0
	v_add_f32_e32 v237, v237, v236
	v_mov_b32_e32 v193, v208
	v_mov_b32_e32 v208, v207
	s_waitcnt lgkmcnt(0)
	s_waitcnt lgkmcnt(0)
	s_waitcnt lgkmcnt(0)
	s_waitcnt lgkmcnt(0)
	s_waitcnt lgkmcnt(0)
	s_waitcnt lgkmcnt(0)
	v_mov_b32_e32 v170, v237
	v_fmamk_f32 v170, v170, 0x3a800000, v167
	v_mul_f32_e32 v192, 0x4b800000, v170
	v_cmp_gt_f32_e32 vcc, s23, v170
	s_nop 1
	v_cndmask_b32_e32 v170, v170, v192, vcc
	v_rsq_f32_e32 v170, v170
	s_nop 0
	v_mul_f32_e32 v192, 0x45800000, v170
	v_cndmask_b32_e32 v170, v170, v192, vcc
	v_mov_b32_e32 v192, v206
	v_pk_mul_f32 v[192:193], v[170:171], v[192:193] op_sel_hi:[0,1]
	v_pk_fma_f32 v[216:217], v[146:147], v[192:193], v[138:139]
	v_pk_mul_f32 v[192:193], v[170:171], v[208:209] op_sel_hi:[0,1]
	v_cvt_pk_fp8_f32 v224, v216, v217
	v_pk_fma_f32 v[208:209], v[14:15], v[216:217], 0 op_sel_hi:[1,0,0]
	v_pk_fma_f32 v[218:219], v[16:17], v[216:217], 0 op_sel_hi:[1,0,0]
	v_pk_fma_f32 v[220:221], v[10:11], v[216:217], 0 op_sel_hi:[1,0,0]
	v_pk_fma_f32 v[222:223], v[12:13], v[216:217], 0 op_sel_hi:[1,0,0]
	v_pk_fma_f32 v[206:207], v[148:149], v[192:193], v[140:141]
	v_pk_fma_f32 v[218:219], v[8:9], v[216:217], v[218:219] op_sel:[0,1,0]
	v_pk_fma_f32 v[208:209], v[6:7], v[216:217], v[208:209] op_sel:[0,1,0]
	v_pk_fma_f32 v[222:223], v[4:5], v[216:217], v[222:223] op_sel:[0,1,0]
	v_pk_fma_f32 v[216:217], v[2:3], v[216:217], v[220:221] op_sel:[0,1,0]
	v_pk_fma_f32 v[208:209], v[30:31], v[206:207], v[208:209] op_sel_hi:[1,0,1]
	v_pk_fma_f32 v[218:219], v[32:33], v[206:207], v[218:219] op_sel_hi:[1,0,1]
	v_pk_fma_f32 v[216:217], v[26:27], v[206:207], v[216:217] op_sel_hi:[1,0,1]
	v_pk_fma_f32 v[220:221], v[28:29], v[206:207], v[222:223] op_sel_hi:[1,0,1]
	v_cvt_pk_fp8_f32 v224, v206, v207 op_sel:[0,0,1]
	v_pk_fma_f32 v[218:219], v[24:25], v[206:207], v[218:219] op_sel:[0,1,0]
	v_pk_fma_f32 v[208:209], v[22:23], v[206:207], v[208:209] op_sel:[0,1,0]
	v_pk_fma_f32 v[220:221], v[20:21], v[206:207], v[220:221] op_sel:[0,1,0]
	v_pk_fma_f32 v[206:207], v[18:19], v[206:207], v[216:217] op_sel:[0,1,0]
	v_mov_b32_e32 v216, v210
	v_mov_b32_e32 v217, v198
	v_pk_mul_f32 v[216:217], v[170:171], v[216:217] op_sel_hi:[0,1]
	v_pk_fma_f32 v[216:217], v[150:151], v[216:217], v[134:135]
	v_mov_b32_e32 v222, 0
	v_mov_b32_e32 v198, v211
	v_cvt_pk_fp8_f32 v222, v216, v217
	v_pk_mul_f32 v[198:199], v[170:171], v[198:199] op_sel_hi:[0,1]
	v_pk_fma_f32 v[208:209], v[46:47], v[216:217], v[208:209] op_sel_hi:[1,0,1]
	v_pk_fma_f32 v[198:199], v[152:153], v[198:199], v[136:137]
	v_pk_fma_f32 v[210:211], v[48:49], v[216:217], v[218:219] op_sel_hi:[1,0,1]
	v_pk_fma_f32 v[206:207], v[42:43], v[216:217], v[206:207] op_sel_hi:[1,0,1]
	v_pk_fma_f32 v[218:219], v[44:45], v[216:217], v[220:221] op_sel_hi:[1,0,1]
	v_pk_fma_f32 v[208:209], v[38:39], v[216:217], v[208:209] op_sel:[0,1,0]
	v_pk_fma_f32 v[210:211], v[40:41], v[216:217], v[210:211] op_sel:[0,1,0]
	v_pk_fma_f32 v[218:219], v[36:37], v[216:217], v[218:219] op_sel:[0,1,0]
	v_pk_fma_f32 v[206:207], v[34:35], v[216:217], v[206:207] op_sel:[0,1,0]
	v_pk_fma_f32 v[208:209], v[50:51], v[198:199], v[208:209] op_sel_hi:[1,0,1]
	v_pk_mul_f32 v[212:213], v[212:213], v[170:171] op_sel_hi:[1,0]
	v_pk_fma_f32 v[210:211], v[52:53], v[198:199], v[210:211] op_sel_hi:[1,0,1]
	v_pk_fma_f32 v[206:207], v[62:63], v[198:199], v[206:207] op_sel_hi:[1,0,1]
	v_pk_fma_f32 v[216:217], v[64:65], v[198:199], v[218:219] op_sel_hi:[1,0,1]
	v_pk_fma_f32 v[208:209], v[58:59], v[198:199], v[208:209] op_sel:[0,1,0]
	v_pk_fma_f32 v[212:213], v[154:155], v[212:213], v[130:131]
	v_cvt_pk_fp8_f32 v222, v198, v199 op_sel:[0,0,1]
	v_pk_fma_f32 v[210:211], v[60:61], v[198:199], v[210:211] op_sel:[0,1,0]
	v_pk_fma_f32 v[216:217], v[56:57], v[198:199], v[216:217] op_sel:[0,1,0]
	v_pk_fma_f32 v[198:199], v[54:55], v[198:199], v[206:207] op_sel:[0,1,0]
	v_pk_mul_f32 v[196:197], v[196:197], v[170:171] op_sel_hi:[1,0]
	v_pk_fma_f32 v[206:207], v[78:79], v[212:213], v[208:209] op_sel_hi:[1,0,1]
	v_mov_b32_e32 v218, 0
	v_pk_fma_f32 v[196:197], v[156:157], v[196:197], v[132:133]
	v_pk_fma_f32 v[208:209], v[80:81], v[212:213], v[210:211] op_sel_hi:[1,0,1]
	v_pk_fma_f32 v[198:199], v[74:75], v[212:213], v[198:199] op_sel_hi:[1,0,1]
	v_pk_fma_f32 v[210:211], v[76:77], v[212:213], v[216:217] op_sel_hi:[1,0,1]
	v_pk_fma_f32 v[206:207], v[70:71], v[212:213], v[206:207] op_sel:[0,1,0]
	v_cvt_pk_fp8_f32 v218, v212, v213
	v_pk_fma_f32 v[208:209], v[72:73], v[212:213], v[208:209] op_sel:[0,1,0]
	v_pk_fma_f32 v[210:211], v[68:69], v[212:213], v[210:211] op_sel:[0,1,0]
	v_pk_fma_f32 v[198:199], v[66:67], v[212:213], v[198:199] op_sel:[0,1,0]
	v_pk_fma_f32 v[206:207], v[82:83], v[196:197], v[206:207] op_sel_hi:[1,0,1]
	v_pk_mul_f32 v[212:213], v[214:215], v[170:171] op_sel_hi:[1,0]
	v_pk_fma_f32 v[206:207], v[90:91], v[196:197], v[206:207] op_sel:[0,1,0]
	v_pk_fma_f32 v[212:213], v[158:159], v[212:213], v[142:143]
	v_pk_mul_f32 v[194:195], v[194:195], v[170:171] op_sel_hi:[1,0]
	v_pk_fma_f32 v[206:207], v[110:111], v[212:213], v[206:207] op_sel_hi:[1,0,1]
	v_pk_fma_f32 v[194:195], v[160:161], v[194:195], v[144:145]
	v_pk_fma_f32 v[206:207], v[102:103], v[212:213], v[206:207] op_sel:[0,1,0]
	v_pk_fma_f32 v[208:209], v[84:85], v[196:197], v[208:209] op_sel_hi:[1,0,1]
	v_pk_fma_f32 v[206:207], v[114:115], v[194:195], v[206:207] op_sel_hi:[1,0,1]
	v_pk_fma_f32 v[198:199], v[94:95], v[196:197], v[198:199] op_sel_hi:[1,0,1]
	v_pk_fma_f32 v[206:207], v[122:123], v[194:195], v[206:207] op_sel:[0,1,0]
	s_nop 1
	v_add_f32_dpp v249, v206, v206 quad_perm:[1,0,3,2] row_mask:0xf bank_mask:0xf
	s_nop 1
	v_add_f32_dpp v249, v249, v249 quad_perm:[2,3,0,1] row_mask:0xf bank_mask:0xf
	s_nop 1
	v_add_f32_dpp v249, v249, v249 row_half_mirror row_mask:0xf bank_mask:0xf
	s_nop 1
	v_add_f32_dpp v249, v249, v249 row_mirror row_mask:0xf bank_mask:0xf
	s_nop 0
	v_mov_b32_e32 v236, v249
	s_nop 1
	v_permlane16_swap_b32_e32 v249, v236
	s_nop 0
	v_add_f32_e32 v249, v249, v236
	v_mov_b32_e32 v236, v249
	s_nop 1
	v_permlane32_swap_b32_e32 v249, v236
	s_nop 0
	v_add_f32_e32 v249, v249, v236
	s_nop 1
	v_add_f32_dpp v248, v207, v207 quad_perm:[1,0,3,2] row_mask:0xf bank_mask:0xf
	s_nop 1
	v_add_f32_dpp v248, v248, v248 quad_perm:[2,3,0,1] row_mask:0xf bank_mask:0xf
	s_nop 1
	v_add_f32_dpp v248, v248, v248 row_half_mirror row_mask:0xf bank_mask:0xf
	s_nop 1
	v_add_f32_dpp v248, v248, v248 row_mirror row_mask:0xf bank_mask:0xf
	s_nop 0
	v_mov_b32_e32 v236, v248
	s_nop 1
	v_permlane16_swap_b32_e32 v248, v236
	s_nop 0
	v_add_f32_e32 v248, v248, v236
	v_mov_b32_e32 v236, v248
	s_nop 1
	v_permlane32_swap_b32_e32 v248, v236
	s_nop 0
	v_add_f32_e32 v248, v248, v236
	v_pk_fma_f32 v[210:211], v[96:97], v[196:197], v[210:211] op_sel_hi:[1,0,1]
	v_pk_fma_f32 v[208:209], v[92:93], v[196:197], v[208:209] op_sel:[0,1,0]
	v_cvt_pk_fp8_f32 v218, v196, v197 op_sel:[0,0,1]
	v_pk_fma_f32 v[210:211], v[88:89], v[196:197], v[210:211] op_sel:[0,1,0]
	s_waitcnt lgkmcnt(0)
	v_pk_fma_f32 v[196:197], v[86:87], v[196:197], v[198:199] op_sel:[0,1,0]
	v_pk_fma_f32 v[198:199], v[112:113], v[212:213], v[208:209] op_sel_hi:[1,0,1]
	v_pk_fma_f32 v[198:199], v[104:105], v[212:213], v[198:199] op_sel:[0,1,0]
	v_mov_b32_e32 v170, 0
	v_pk_fma_f32 v[198:199], v[116:117], v[194:195], v[198:199] op_sel_hi:[1,0,1]
	v_cvt_pk_fp8_f32 v170, v212, v213
	s_waitcnt lgkmcnt(0)
	v_pk_fma_f32 v[198:199], v[124:125], v[194:195], v[198:199] op_sel:[0,1,0]
	s_nop 1
	v_add_f32_dpp v237, v198, v198 quad_perm:[1,0,3,2] row_mask:0xf bank_mask:0xf
	s_nop 1
	v_add_f32_dpp v237, v237, v237 quad_perm:[2,3,0,1] row_mask:0xf bank_mask:0xf
	s_nop 1
	v_add_f32_dpp v237, v237, v237 row_half_mirror row_mask:0xf bank_mask:0xf
	s_nop 1
	v_add_f32_dpp v237, v237, v237 row_mirror row_mask:0xf bank_mask:0xf
	s_nop 0
	v_mov_b32_e32 v236, v237
	s_nop 1
	v_permlane16_swap_b32_e32 v237, v236
	s_nop 0
	v_add_f32_e32 v237, v237, v236
	v_mov_b32_e32 v236, v237
	s_nop 1
	v_permlane32_swap_b32_e32 v237, v236
	s_nop 0
	v_add_f32_e32 v237, v237, v236
	v_pk_fma_f32 v[196:197], v[106:107], v[212:213], v[196:197] op_sel_hi:[1,0,1]
	v_pk_fma_f32 v[210:211], v[108:109], v[212:213], v[210:211] op_sel_hi:[1,0,1]
	s_waitcnt lgkmcnt(1)
	s_waitcnt lgkmcnt(2)
	v_pk_fma_f32 v[210:211], v[100:101], v[212:213], v[210:211] op_sel:[0,1,0]
	v_pk_fma_f32 v[196:197], v[98:99], v[212:213], v[196:197] op_sel:[0,1,0]
	v_pk_fma_f32 v[210:211], v[128:129], v[194:195], v[210:211] op_sel_hi:[1,0,1]
	v_pk_fma_f32 v[196:197], v[126:127], v[194:195], v[196:197] op_sel_hi:[1,0,1]
	v_cvt_pk_fp8_f32 v170, v194, v195 op_sel:[0,0,1]
	v_pk_fma_f32 v[210:211], v[120:121], v[194:195], v[210:211] op_sel:[0,1,0]
	v_pk_fma_f32 v[212:213], v[118:119], v[194:195], v[196:197] op_sel:[0,1,0]
	s_waitcnt lgkmcnt(1)
	s_nop 1
	v_add_f32_dpp v238, v199, v199 quad_perm:[1,0,3,2] row_mask:0xf bank_mask:0xf
	s_nop 1
	v_add_f32_dpp v238, v238, v238 quad_perm:[2,3,0,1] row_mask:0xf bank_mask:0xf
	s_nop 1
	v_add_f32_dpp v238, v238, v238 row_half_mirror row_mask:0xf bank_mask:0xf
	s_nop 1
	v_add_f32_dpp v238, v238, v238 row_mirror row_mask:0xf bank_mask:0xf
	s_nop 0
	v_mov_b32_e32 v236, v238
	s_nop 1
	v_permlane16_swap_b32_e32 v238, v236
	s_nop 0
	v_add_f32_e32 v238, v238, v236
	v_mov_b32_e32 v236, v238
	s_nop 1
	v_permlane32_swap_b32_e32 v238, v236
	s_nop 0
	v_add_f32_e32 v238, v238, v236
	s_waitcnt lgkmcnt(3)
	s_nop 1
	v_add_f32_dpp v239, v212, v212 quad_perm:[1,0,3,2] row_mask:0xf bank_mask:0xf
	s_nop 1
	v_add_f32_dpp v239, v239, v239 quad_perm:[2,3,0,1] row_mask:0xf bank_mask:0xf
	s_nop 1
	v_add_f32_dpp v239, v239, v239 row_half_mirror row_mask:0xf bank_mask:0xf
	s_nop 1
	v_add_f32_dpp v239, v239, v239 row_mirror row_mask:0xf bank_mask:0xf
	s_nop 0
	v_mov_b32_e32 v236, v239
	s_nop 1
	v_permlane16_swap_b32_e32 v239, v236
	s_nop 0
	v_add_f32_e32 v239, v239, v236
	v_mov_b32_e32 v236, v239
	s_nop 1
	v_permlane32_swap_b32_e32 v239, v236
	s_nop 0
	v_add_f32_e32 v239, v239, v236
	s_waitcnt lgkmcnt(3)
	s_waitcnt lgkmcnt(2)
	s_waitcnt lgkmcnt(2)
	s_waitcnt lgkmcnt(1)
	s_waitcnt lgkmcnt(2)
	s_nop 1
	v_add_f32_dpp v240, v213, v213 quad_perm:[1,0,3,2] row_mask:0xf bank_mask:0xf
	s_nop 1
	v_add_f32_dpp v240, v240, v240 quad_perm:[2,3,0,1] row_mask:0xf bank_mask:0xf
	s_nop 1
	v_add_f32_dpp v240, v240, v240 row_half_mirror row_mask:0xf bank_mask:0xf
	s_nop 1
	v_add_f32_dpp v240, v240, v240 row_mirror row_mask:0xf bank_mask:0xf
	s_nop 0
	v_mov_b32_e32 v236, v240
	s_nop 1
	v_permlane16_swap_b32_e32 v240, v236
	s_nop 0
	v_add_f32_e32 v240, v240, v236
	v_mov_b32_e32 v236, v240
	s_nop 1
	v_permlane32_swap_b32_e32 v240, v236
	s_nop 0
	v_add_f32_e32 v240, v240, v236
	s_waitcnt lgkmcnt(3)
	s_waitcnt lgkmcnt(3)
	s_waitcnt lgkmcnt(2)
	s_waitcnt lgkmcnt(2)
	s_nop 1
	v_add_f32_dpp v241, v211, v211 quad_perm:[1,0,3,2] row_mask:0xf bank_mask:0xf
	s_nop 1
	v_add_f32_dpp v241, v241, v241 quad_perm:[2,3,0,1] row_mask:0xf bank_mask:0xf
	s_nop 1
	v_add_f32_dpp v241, v241, v241 row_half_mirror row_mask:0xf bank_mask:0xf
	s_nop 1
	v_add_f32_dpp v241, v241, v241 row_mirror row_mask:0xf bank_mask:0xf
	s_nop 0
	v_mov_b32_e32 v236, v241
	s_nop 1
	v_permlane16_swap_b32_e32 v241, v236
	s_nop 0
	v_add_f32_e32 v241, v241, v236
	v_mov_b32_e32 v236, v241
	s_nop 1
	v_permlane32_swap_b32_e32 v241, v236
	s_nop 0
	v_add_f32_e32 v241, v241, v236
	s_waitcnt lgkmcnt(3)
	s_waitcnt lgkmcnt(2)
	s_waitcnt lgkmcnt(2)
	s_waitcnt lgkmcnt(2)
	s_waitcnt lgkmcnt(1)
	s_waitcnt lgkmcnt(1)
	s_nop 1
	v_add_f32_dpp v242, v210, v210 quad_perm:[1,0,3,2] row_mask:0xf bank_mask:0xf
	s_nop 1
	v_add_f32_dpp v242, v242, v242 quad_perm:[2,3,0,1] row_mask:0xf bank_mask:0xf
	s_nop 1
	v_add_f32_dpp v242, v242, v242 row_half_mirror row_mask:0xf bank_mask:0xf
	s_nop 1
	v_add_f32_dpp v242, v242, v242 row_mirror row_mask:0xf bank_mask:0xf
	s_nop 0
	v_mov_b32_e32 v236, v242
	s_nop 1
	v_permlane16_swap_b32_e32 v242, v236
	s_nop 0
	v_add_f32_e32 v242, v242, v236
	v_mov_b32_e32 v236, v242
	s_nop 1
	v_permlane32_swap_b32_e32 v242, v236
	s_nop 0
	v_add_f32_e32 v242, v242, v236
	s_waitcnt lgkmcnt(3)
	s_waitcnt lgkmcnt(3)
	s_waitcnt lgkmcnt(3)
	s_waitcnt lgkmcnt(2)
	s_waitcnt lgkmcnt(2)
	s_waitcnt lgkmcnt(2)
	s_waitcnt lgkmcnt(2)
	s_waitcnt lgkmcnt(2)
	s_waitcnt lgkmcnt(2)
	s_waitcnt lgkmcnt(3)
	s_waitcnt lgkmcnt(3)
	s_waitcnt lgkmcnt(2)
	v_lshl_add_u64 v[192:193], s[72:73], 0, v[180:181]
	v_add_co_u32_e32 v192, vcc, s35, v192
	s_nop 1
	v_addc_co_u32_e32 v193, vcc, 0, v193, vcc
	global_store_dword v[192:193], v224, off
	global_store_dword v[192:193], v222, off offset:256
	global_store_dword v[192:193], v218, off offset:512
	global_store_dword v[192:193], v170, off offset:768
	s_and_saveexec_b64 s[44:45], s[4:5]
	s_cbranch_execz .LBB0_1747
	v_mov_b32_e32 v192, v249
	v_mov_b32_e32 v193, v248
	v_mov_b32_e32 v198, v237
	v_cmp_gt_f32_e32 vcc, v193, v192
	s_waitcnt lgkmcnt(4)
	v_mov_b32_e32 v201, v238
	s_waitcnt lgkmcnt(3)
	v_mov_b32_e32 v206, v239
	v_cndmask_b32_e32 v194, v192, v193, vcc
	v_cmp_gt_f32_e64 s[6:7], v198, v194
	s_waitcnt lgkmcnt(2)
	v_mov_b32_e32 v208, v240
	v_cndmask_b32_e64 v195, 0, 1, vcc
	v_cndmask_b32_e64 v194, v194, v198, s[6:7]
	v_cmp_gt_f32_e64 s[8:9], v201, v194
	v_cndmask_b32_e64 v195, v195, 2, s[6:7]
	s_waitcnt lgkmcnt(1)
	v_mov_b32_e32 v210, v242
	v_cndmask_b32_e64 v194, v194, v201, s[8:9]
	v_cmp_gt_f32_e64 s[10:11], v206, v194
	v_cndmask_b32_e64 v195, v195, 3, s[8:9]
	s_waitcnt lgkmcnt(0)
	v_mov_b32_e32 v170, v241
	v_cndmask_b32_e64 v194, v194, v206, s[10:11]
	v_cmp_gt_f32_e64 s[12:13], v208, v194
	v_cndmask_b32_e64 v195, v195, 4, s[10:11]
	s_ashr_i32 s39, s38, 31
	v_cndmask_b32_e64 v194, v194, v208, s[12:13]
	v_cmp_gt_f32_e64 s[14:15], v210, v194
	v_cndmask_b32_e64 v195, v195, 5, s[12:13]
	s_lshl_b64 s[6:7], s[38:39], 2
	v_cndmask_b32_e64 v194, v194, v210, s[14:15]
	v_cmp_ngt_f32_e64 s[16:17], v170, v194
	v_cndmask_b32_e64 v195, v195, 6, s[14:15]
	s_and_b64 s[20:21], s[14:15], s[16:17]
	v_cndmask_b32_e64 v195, 7, v195, s[16:17]
	v_cmp_nlt_f32_e32 vcc, s46, v192
	s_add_u32 s48, s30, s6
	v_cmp_eq_u32_e64 s[18:19], 0, v195
	s_addc_u32 s49, s31, s7
	s_or_b64 vcc, s[18:19], vcc
	v_cndmask_b32_e32 v192, v192, v177, vcc
	v_cmp_ne_u32_e64 s[14:15], 1, v195
	v_cmp_gt_f32_e64 s[18:19], v193, v192
	s_and_b64 s[14:15], s[14:15], s[18:19]
	v_cndmask_b32_e64 v192, v192, v193, s[14:15]
	v_cmp_ne_u32_e64 s[12:13], 2, v195
	v_cmp_gt_f32_e64 s[18:19], v198, v192
	s_and_b64 s[12:13], s[12:13], s[18:19]
	v_cndmask_b32_e64 v192, v192, v198, s[12:13]
	v_cmp_ne_u32_e64 s[10:11], 3, v195
	v_cmp_gt_f32_e64 s[18:19], v201, v192
	s_and_b64 s[10:11], s[10:11], s[18:19]
	v_cndmask_b32_e64 v192, v192, v201, s[10:11]
	v_cmp_ne_u32_e64 s[8:9], 4, v195
	v_cmp_gt_f32_e64 s[18:19], v206, v192
	s_and_b64 s[8:9], s[8:9], s[18:19]
	v_cndmask_b32_e64 v192, v192, v206, s[8:9]
	v_cmp_ne_u32_e64 s[6:7], 5, v195
	v_cmp_gt_f32_e64 s[18:19], v208, v192
	s_and_b64 s[6:7], s[6:7], s[18:19]
	v_cndmask_b32_e64 v192, v192, v208, s[6:7]
	v_cmp_ngt_f32_e64 s[18:19], v210, v192
	s_or_b64 s[18:19], s[20:21], s[18:19]
	v_cndmask_b32_e64 v194, v170, v194, s[16:17]
	v_cndmask_b32_e64 v192, v210, v192, s[18:19]
	v_cmp_gt_f32_e64 s[20:21], v170, v192
	s_and_b64 s[16:17], s[16:17], s[20:21]
	v_cndmask_b32_e64 v170, v192, v170, s[16:17]
	v_sub_f32_e32 v170, v170, v194
	v_mul_f32_e32 v170, 0x3fb8aa3b, v170
	v_exp_f32_e32 v170, v170
	v_cndmask_b32_e64 v192, 0, -1, vcc
	v_cndmask_b32_e64 v192, v192, 1, s[14:15]
	v_cndmask_b32_e64 v192, v192, 2, s[12:13]
	v_cndmask_b32_e64 v192, v192, 3, s[10:11]
	v_add_f32_e32 v170, 1.0, v170
	v_cndmask_b32_e64 v192, v192, 4, s[8:9]
	v_div_scale_f32 v193, s[8:9], v170, v170, 1.0
	v_rcp_f32_e32 v194, v193
	v_cndmask_b32_e64 v192, v192, 5, s[6:7]
	v_cndmask_b32_e64 v192, 6, v192, s[18:19]
	v_cndmask_b32_e64 v196, v192, 7, s[16:17]
	v_fma_f32 v192, -v193, v194, 1.0
	v_fmac_f32_e32 v194, v192, v194
	v_div_scale_f32 v192, vcc, 1.0, v170, 1.0
	v_mul_f32_e32 v197, v192, v194
	v_fma_f32 v198, -v193, v197, v192
	v_fmac_f32_e32 v197, v198, v194
	v_fma_f32 v192, -v193, v197, v192
	v_div_fmas_f32 v192, v192, v194, v197
	v_div_fixup_f32 v192, v192, v170, 1.0
	v_sub_f32_e32 v193, 1.0, v192
	global_store_dwordx2 v163, v[192:193], s[48:49]
	v_lshl_add_u32 v170, v195, 2, 0
	ds_add_rtn_u32 v170, v170, v173
	v_lshl_add_u32 v192, v196, 2, 0
	ds_add_rtn_u32 v192, v192, v173
	s_min_i32 s39, s33, 63
	s_lshl_b32 s6, s39, 3
	s_add_i32 s6, s34, s6
	v_lshlrev_b32_e32 v193, 16, v196
	v_lshlrev_b32_e32 v194, 16, v195
	s_waitcnt lgkmcnt(0)
	v_or_b32_e32 v193, v192, v193
	v_or_b32_e32 v192, v170, v194
	v_mov_b32_e32 v170, s6
	ds_write_b64 v170, v[192:193] offset:64
	s_branch .LBB0_1747
